# small_proj block prologue: both H-tile halves and the first weight set loaded in one batch with counted waits (three serialized round trips become one)
# baseline (speedup 1.0000x reference)
.LBB0_360:
	s_lshl_b32 s15, s14, 5
	v_add_u32_e32 v0, s15, v103
	v_add_u32_e32 v4, s15, v104
	v_add_u32_e32 v8, s15, v105
	v_add_u32_e32 v12, s15, v106
	v_add_u32_e32 v16, s15, v107
	v_add_u32_e32 v20, s15, v108
	v_add_u32_e32 v24, s15, v109
	v_add_u32_e32 v28, s15, v110
	v_ashrrev_i32_e32 v1, 31, v0
	v_ashrrev_i32_e32 v5, 31, v4
	v_ashrrev_i32_e32 v9, 31, v8
	v_ashrrev_i32_e32 v13, 31, v12
	v_ashrrev_i32_e32 v17, 31, v16
	v_ashrrev_i32_e32 v21, 31, v20
	v_ashrrev_i32_e32 v25, 31, v24
	v_ashrrev_i32_e32 v29, 31, v28
	v_lshlrev_b64 v[0:1], 12, v[0:1]
	v_lshlrev_b64 v[4:5], 12, v[4:5]
	v_lshlrev_b64 v[8:9], 12, v[8:9]
	v_lshlrev_b64 v[12:13], 12, v[12:13]
	v_lshlrev_b64 v[16:17], 12, v[16:17]
	v_lshlrev_b64 v[20:21], 12, v[20:21]
	v_lshlrev_b64 v[24:25], 12, v[24:25]
	v_lshlrev_b64 v[28:29], 12, v[28:29]
	v_lshl_add_u64 v[0:1], v[82:83], 0, v[0:1]
	v_lshl_add_u64 v[4:5], v[82:83], 0, v[4:5]
	v_lshl_add_u64 v[8:9], v[82:83], 0, v[8:9]
	v_lshl_add_u64 v[12:13], v[82:83], 0, v[12:13]
	v_lshl_add_u64 v[16:17], v[82:83], 0, v[16:17]
	v_lshl_add_u64 v[20:21], v[82:83], 0, v[20:21]
	v_lshl_add_u64 v[24:25], v[82:83], 0, v[24:25]
	v_lshl_add_u64 v[28:29], v[82:83], 0, v[28:29]
	s_barrier
	global_load_dwordx4 v[0:3], v[0:1], off
	s_mov_b32 s4, 0
	global_load_dwordx4 v[4:7], v[4:5], off
	v_mov_b32_e32 v46, v102
	global_load_dwordx4 v[8:11], v[8:9], off
	s_nop 0
	global_load_dwordx4 v[12:15], v[12:13], off
	s_nop 0
	global_load_dwordx4 v[16:19], v[16:17], off
	s_nop 0
	global_load_dwordx4 v[20:23], v[20:21], off
	s_nop 0
	global_load_dwordx4 v[24:27], v[24:25], off
	s_nop 0
	global_load_dwordx4 v[28:31], v[28:29], off
	v_add_u32_e32 v186, s15, v111
	v_add_u32_e32 v188, s15, v112
	v_add_u32_e32 v190, s15, v113
	v_add_u32_e32 v192, s15, v114
	v_add_u32_e32 v194, s15, v115
	v_add_u32_e32 v196, s15, v116
	v_add_u32_e32 v198, s15, v117
	v_add_u32_e32 v200, s15, v118
	v_ashrrev_i32_e32 v187, 31, v186
	v_ashrrev_i32_e32 v189, 31, v188
	v_ashrrev_i32_e32 v191, 31, v190
	v_ashrrev_i32_e32 v193, 31, v192
	v_ashrrev_i32_e32 v195, 31, v194
	v_ashrrev_i32_e32 v197, 31, v196
	v_ashrrev_i32_e32 v199, 31, v198
	v_ashrrev_i32_e32 v201, 31, v200
	v_lshlrev_b64 v[186:187], 12, v[186:187]
	v_lshlrev_b64 v[188:189], 12, v[188:189]
	v_lshlrev_b64 v[190:191], 12, v[190:191]
	v_lshlrev_b64 v[192:193], 12, v[192:193]
	v_lshlrev_b64 v[194:195], 12, v[194:195]
	v_lshlrev_b64 v[196:197], 12, v[196:197]
	v_lshlrev_b64 v[198:199], 12, v[198:199]
	v_lshlrev_b64 v[200:201], 12, v[200:201]
	v_lshl_add_u64 v[186:187], v[82:83], 0, v[186:187]
	v_lshl_add_u64 v[188:189], v[82:83], 0, v[188:189]
	v_lshl_add_u64 v[190:191], v[82:83], 0, v[190:191]
	v_lshl_add_u64 v[192:193], v[82:83], 0, v[192:193]
	v_lshl_add_u64 v[194:195], v[82:83], 0, v[194:195]
	v_lshl_add_u64 v[196:197], v[82:83], 0, v[196:197]
	v_lshl_add_u64 v[198:199], v[82:83], 0, v[198:199]
	v_lshl_add_u64 v[200:201], v[82:83], 0, v[200:201]
	global_load_dwordx4 v[48:51], v[186:187], off
	global_load_dwordx4 v[52:55], v[188:189], off
	global_load_dwordx4 v[56:59], v[190:191], off
	global_load_dwordx4 v[60:63], v[192:193], off
	global_load_dwordx4 v[64:67], v[194:195], off
	global_load_dwordx4 v[172:175], v[196:197], off
	global_load_dwordx4 v[176:179], v[198:199], off
	global_load_dwordx4 v[180:183], v[200:201], off
	global_load_dwordx4 v[140:143], v[88:89], off
	global_load_dwordx4 v[144:147], v[88:89], off offset:64
	global_load_dwordx4 v[148:151], v[88:89], off offset:128
	global_load_dwordx4 v[152:155], v[88:89], off offset:192
	global_load_dwordx4 v[156:159], v[88:89], off offset:256
	global_load_dwordx4 v[160:163], v[88:89], off offset:320
	global_load_dwordx4 v[164:167], v[88:89], off offset:384
	global_load_dwordx4 v[168:171], v[88:89], off offset:448
	s_waitcnt vmcnt(16)
	ds_write_b128 v32, v[0:3]
	ds_write_b128 v87, v[4:7]
	ds_write_b128 v119, v[8:11]
	ds_write_b128 v120, v[12:15]
	ds_write_b128 v121, v[16:19]
	ds_write_b128 v122, v[20:23]
	ds_write_b128 v123, v[24:27]
	ds_write_b128 v124, v[28:31]
	s_waitcnt vmcnt(8)
	ds_write_b128 v125, v[48:51]
	ds_write_b128 v126, v[52:55]
	ds_write_b128 v127, v[56:59]
	ds_write_b128 v128, v[60:63]
	ds_write_b128 v129, v[64:67]
	ds_write_b128 v130, v[172:175]
	ds_write_b128 v131, v[176:179]
	ds_write_b128 v132, v[180:183]
	s_waitcnt lgkmcnt(0)
	s_barrier
	s_waitcnt vmcnt(0)
	v_mov_b64_e32 v[42:43], v[140:141]
	v_mov_b64_e32 v[44:45], v[142:143]
	v_mov_b64_e32 v[38:39], v[144:145]
	v_mov_b64_e32 v[40:41], v[146:147]
	v_mov_b64_e32 v[28:29], v[148:149]
	v_mov_b64_e32 v[30:31], v[150:151]
	v_mov_b64_e32 v[24:25], v[152:153]
	v_mov_b64_e32 v[26:27], v[154:155]
	v_mov_b64_e32 v[20:21], v[156:157]
	v_mov_b64_e32 v[22:23], v[158:159]
	v_mov_b64_e32 v[16:17], v[160:161]
	v_mov_b64_e32 v[18:19], v[162:163]
	v_mov_b64_e32 v[12:13], v[164:165]
	v_mov_b64_e32 v[14:15], v[166:167]
	v_mov_b64_e32 v[8:9], v[168:169]
	v_mov_b64_e32 v[10:11], v[170:171]
	v_mov_b32_e32 v4, 0
	v_mov_b32_e32 v5, v4
	v_mov_b32_e32 v6, v4
	v_mov_b32_e32 v7, v4
	v_mov_b32_e32 v0, v4
	v_mov_b32_e32 v1, v4
	v_mov_b32_e32 v2, v4
	v_mov_b32_e32 v3, v4
